# pool phase: second pool-scale load issued with the first (counted waits), on top of NA bias hoist
# speedup vs baseline: 1.0036x; 1.0036x over previous
.LBB0_355:
	s_or_b64 exec, exec, s[24:25]
	v_sub_u32_e32 v8, v26, v8
	v_cvt_f32_i32_e32 v8, v8
	ds_read_b128 v[26:29], v15 offset:2048
	ds_read_b128 v[30:33], v15 offset:2064
	s_lshl_b32 s20, s47, 7
	s_lshl_b32 s26, s47, 8
	v_div_scale_f32 v34, s[24:25], v8, v8, 1.0
	v_rcp_f32_e32 v35, v34
	v_div_scale_f32 v36, vcc, 1.0, v8, 1.0
	v_lshlrev_b32_e32 v44, 2, v6
	v_fma_f32 v37, -v34, v35, 1.0
	v_fmac_f32_e32 v35, v37, v35
	v_mul_f32_e32 v37, v36, v35
	v_fma_f32 v38, -v34, v37, v36
	v_fmac_f32_e32 v37, v38, v35
	v_fma_f32 v34, -v34, v37, v36
	v_div_fmas_f32 v34, v34, v35, v37
	v_div_fixup_f32 v8, v34, v8, 1.0
	s_waitcnt lgkmcnt(1)
	v_pk_fma_f32 v[10:11], v[8:9], v[10:11], v[26:27] op_sel_hi:[0,1,1] neg_lo:[0,0,1] neg_hi:[0,0,1]
	v_pk_fma_f32 v[12:13], v[8:9], v[12:13], v[28:29] op_sel_hi:[0,1,1] neg_lo:[0,0,1] neg_hi:[0,0,1]
	s_waitcnt lgkmcnt(0)
	v_pk_fma_f32 v[4:5], v[8:9], v[4:5], v[30:31] op_sel_hi:[0,1,1] neg_lo:[0,0,1] neg_hi:[0,0,1]
	v_pk_fma_f32 v[2:3], v[8:9], v[2:3], v[32:33] op_sel_hi:[0,1,1] neg_lo:[0,0,1] neg_hi:[0,0,1]
	v_cvt_pk_f16_f32 v10, v10, v11
	v_cvt_pk_f16_f32 v11, v12, v13
	v_cvt_pk_f16_f32 v12, v4, v5
	v_cvt_pk_f16_f32 v13, v2, v3
	v_mov_b32_e32 v2, s43
	ds_write_b128 v16, v[10:13] offset:20480
	s_waitcnt lgkmcnt(0)
	s_barrier
	ds_read_b64 v[10:11], v2
	ds_read_b128 v[26:29], v24 offset:29696
	v_add_u32_e32 v38, s46, v17
	ds_read_b128 v[2:5], v25 offset:29696
	v_ashrrev_i32_e32 v39, 31, v38
	s_waitcnt lgkmcnt(2)
	v_readfirstlane_b32 s24, v10
	v_readfirstlane_b32 s25, v11
	s_add_u32 s24, s24, s26
	s_addc_u32 s25, s25, 0
	s_lshl_b32 s26, s36, 2
	s_add_u32 s24, s24, s26
	s_addc_u32 s25, s25, 0
	global_load_dwordx4 v[10:13], v44, s[24:25]
	global_load_dwordx4 v[226:229], v44, s[24:25] offset:64
	ds_read_b128 v[30:33], v23 offset:20480
	ds_read_b128 v[34:37], v24 offset:29760
	v_lshlrev_b64 v[38:39], 11, v[38:39]
	v_lshl_add_u64 v[38:39], s[18:19], 0, v[38:39]
	v_lshl_add_u64 v[42:43], v[38:39], 0, s[20:21]
	ds_read_b128 v[38:41], v23 offset:20544
	s_waitcnt lgkmcnt(2)
	v_mfma_f32_16x16x32_f16 v[26:29], v[26:29], v[30:33], 0
	v_lshlrev_b32_e32 v8, 1, v6
	v_lshl_add_u64 v[42:43], v[42:43], 0, v[8:9]
	s_lshl_b32 s20, s36, 1
	s_waitcnt lgkmcnt(0)
	v_mfma_f32_16x16x32_f16 v[26:29], v[34:37], v[38:41], v[26:29]
	v_lshl_add_u64 v[42:43], v[42:43], 0, s[20:21]
	s_add_i32 s45, s45, s33
	s_add_i32 s44, s44, s33
	v_mfma_f32_16x16x32_f16 v[2:5], v[2:5], v[30:33], 0
	s_add_i32 s37, s37, s38
	s_cmpk_gt_i32 s45, 0x47f
	s_waitcnt vmcnt(1)
	s_nop 0
	v_mul_f32_e32 v8, v28, v12
	v_mul_f32_e32 v11, v27, v11
	v_fma_mixlo_f16 v26, v26, v10, 0
	v_pk_mov_b32 v[10:11], v[10:11], v[8:9] op_sel:[1,0]
	v_fma_mixlo_f16 v12, v29, v13, 0
	v_cvt_pk_f16_f32 v8, v10, v11
	v_pack_b32_f16 v10, v26, v8
	v_alignbit_b32 v11, v12, v8, 16
	global_store_dwordx2 v[42:43], v[10:11], off
	ds_read_b128 v[26:29], v25 offset:29760
	s_waitcnt lgkmcnt(0)
	v_mfma_f32_16x16x32_f16 v[2:5], v[26:29], v[38:41], v[2:5]
	s_waitcnt vmcnt(1)
	s_nop 6
	v_fma_mixlo_f16 v8, v2, v226, 0
	v_mul_f32_e32 v2, v4, v228
	v_mul_f32_e32 v3, v3, v227
	v_pk_mov_b32 v[2:3], v[2:3], v[2:3] op_sel:[1,0]
	v_fma_mixlo_f16 v4, v5, v229, 0
	v_cvt_pk_f16_f32 v3, v2, v3
	v_pack_b32_f16 v2, v8, v3
	v_alignbit_b32 v3, v4, v3, 16
	global_store_dwordx2 v[42:43], v[2:3], off offset:32
	s_cbranch_scc1 .LBB0_384

.LBB0_1753:
	s_or_b64 exec, exec, s[26:27]
	v_sub_u32_e32 v8, v26, v8
	v_cvt_f32_i32_e32 v8, v8
	ds_read_b128 v[26:29], v15 offset:2048
	ds_read_b128 v[30:33], v15 offset:2064
	s_lshl_b32 s20, s49, 7
	s_lshl_b32 s28, s49, 8
	v_div_scale_f32 v34, s[26:27], v8, v8, 1.0
	v_rcp_f32_e32 v35, v34
	v_div_scale_f32 v36, vcc, 1.0, v8, 1.0
	v_lshlrev_b32_e32 v44, 2, v6
	v_fma_f32 v37, -v34, v35, 1.0
	v_fmac_f32_e32 v35, v37, v35
	v_mul_f32_e32 v37, v36, v35
	v_fma_f32 v38, -v34, v37, v36
	v_fmac_f32_e32 v37, v38, v35
	v_fma_f32 v34, -v34, v37, v36
	v_div_fmas_f32 v34, v34, v35, v37
	v_div_fixup_f32 v8, v34, v8, 1.0
	s_waitcnt lgkmcnt(1)
	v_pk_fma_f32 v[10:11], v[8:9], v[10:11], v[26:27] op_sel_hi:[0,1,1] neg_lo:[0,0,1] neg_hi:[0,0,1]
	v_pk_fma_f32 v[12:13], v[8:9], v[12:13], v[28:29] op_sel_hi:[0,1,1] neg_lo:[0,0,1] neg_hi:[0,0,1]
	s_waitcnt lgkmcnt(0)
	v_pk_fma_f32 v[4:5], v[8:9], v[4:5], v[30:31] op_sel_hi:[0,1,1] neg_lo:[0,0,1] neg_hi:[0,0,1]
	v_pk_fma_f32 v[2:3], v[8:9], v[2:3], v[32:33] op_sel_hi:[0,1,1] neg_lo:[0,0,1] neg_hi:[0,0,1]
	v_cvt_pk_f16_f32 v10, v10, v11
	v_cvt_pk_f16_f32 v11, v12, v13
	v_cvt_pk_f16_f32 v12, v4, v5
	v_cvt_pk_f16_f32 v13, v2, v3
	v_mov_b32_e32 v2, s45
	ds_write_b128 v16, v[10:13] offset:20480
	s_waitcnt lgkmcnt(0)
	s_barrier
	ds_read_b64 v[10:11], v2
	ds_read_b128 v[26:29], v24 offset:29696
	v_add_u32_e32 v38, s48, v17
	ds_read_b128 v[2:5], v25 offset:29696
	v_ashrrev_i32_e32 v39, 31, v38
	s_waitcnt lgkmcnt(2)
	v_readfirstlane_b32 s26, v10
	v_readfirstlane_b32 s27, v11
	s_add_u32 s26, s26, s28
	s_addc_u32 s27, s27, 0
	s_lshl_b32 s28, s38, 2
	s_add_u32 s26, s26, s28
	s_addc_u32 s27, s27, 0
	global_load_dwordx4 v[10:13], v44, s[26:27] offset:1024
	global_load_dwordx4 v[226:229], v44, s[26:27] offset:1088
	ds_read_b128 v[30:33], v23 offset:20480
	ds_read_b128 v[34:37], v24 offset:29760
	v_lshlrev_b64 v[38:39], 11, v[38:39]
	v_lshl_add_u64 v[38:39], s[18:19], 0, v[38:39]
	v_lshl_add_u64 v[42:43], v[38:39], 0, s[20:21]
	ds_read_b128 v[38:41], v23 offset:20544
	s_waitcnt lgkmcnt(2)
	v_mfma_f32_16x16x32_f16 v[26:29], v[26:29], v[30:33], 0
	v_lshlrev_b32_e32 v8, 1, v6
	v_lshl_add_u64 v[42:43], v[42:43], 0, v[8:9]
	s_lshl_b32 s20, s38, 1
	s_waitcnt lgkmcnt(0)
	v_mfma_f32_16x16x32_f16 v[26:29], v[34:37], v[38:41], v[26:29]
	v_lshl_add_u64 v[42:43], v[42:43], 0, s[20:21]
	s_add_i32 s47, s47, s33
	s_add_i32 s46, s46, s33
	v_mfma_f32_16x16x32_f16 v[2:5], v[2:5], v[30:33], 0
	s_add_i32 s39, s39, s40
	s_cmpk_gt_i32 s47, 0x47f
	s_waitcnt vmcnt(1)
	s_nop 0
	v_mul_f32_e32 v8, v28, v12
	v_mul_f32_e32 v11, v27, v11
	v_fma_mixlo_f16 v26, v26, v10, 0
	v_pk_mov_b32 v[10:11], v[10:11], v[8:9] op_sel:[1,0]
	v_fma_mixlo_f16 v12, v29, v13, 0
	v_cvt_pk_f16_f32 v8, v10, v11
	v_pack_b32_f16 v10, v26, v8
	v_alignbit_b32 v11, v12, v8, 16
	global_store_dwordx2 v[42:43], v[10:11], off
	ds_read_b128 v[26:29], v25 offset:29760
	s_waitcnt lgkmcnt(0)
	v_mfma_f32_16x16x32_f16 v[2:5], v[26:29], v[38:41], v[2:5]
	s_waitcnt vmcnt(1)
	s_nop 6
	v_fma_mixlo_f16 v8, v2, v226, 0
	v_mul_f32_e32 v2, v4, v228
	v_mul_f32_e32 v3, v3, v227
	v_pk_mov_b32 v[2:3], v[2:3], v[2:3] op_sel:[1,0]
	v_fma_mixlo_f16 v4, v5, v229, 0
	v_cvt_pk_f16_f32 v3, v2, v3
	v_pack_b32_f16 v2, v8, v3
	v_alignbit_b32 v3, v4, v3, 16
	global_store_dwordx2 v[42:43], v[2:3], off offset:32
	s_cbranch_scc1 .LBB0_1782

.LBB0_3372:
	s_or_b64 exec, exec, s[26:27]
	v_sub_u32_e32 v8, v26, v8
	v_cvt_f32_i32_e32 v8, v8
	ds_read_b128 v[26:29], v15 offset:2048
	ds_read_b128 v[30:33], v15 offset:2064
	s_lshl_b32 s20, s49, 7
	s_lshl_b32 s28, s49, 8
	v_div_scale_f32 v34, s[26:27], v8, v8, 1.0
	v_rcp_f32_e32 v35, v34
	v_div_scale_f32 v36, vcc, 1.0, v8, 1.0
	v_lshlrev_b32_e32 v44, 2, v6
	v_fma_f32 v37, -v34, v35, 1.0
	v_fmac_f32_e32 v35, v37, v35
	v_mul_f32_e32 v37, v36, v35
	v_fma_f32 v38, -v34, v37, v36
	v_fmac_f32_e32 v37, v38, v35
	v_fma_f32 v34, -v34, v37, v36
	v_div_fmas_f32 v34, v34, v35, v37
	v_div_fixup_f32 v8, v34, v8, 1.0
	s_waitcnt lgkmcnt(1)
	v_pk_fma_f32 v[10:11], v[8:9], v[10:11], v[26:27] op_sel_hi:[0,1,1] neg_lo:[0,0,1] neg_hi:[0,0,1]
	v_pk_fma_f32 v[12:13], v[8:9], v[12:13], v[28:29] op_sel_hi:[0,1,1] neg_lo:[0,0,1] neg_hi:[0,0,1]
	s_waitcnt lgkmcnt(0)
	v_pk_fma_f32 v[4:5], v[8:9], v[4:5], v[30:31] op_sel_hi:[0,1,1] neg_lo:[0,0,1] neg_hi:[0,0,1]
	v_pk_fma_f32 v[2:3], v[8:9], v[2:3], v[32:33] op_sel_hi:[0,1,1] neg_lo:[0,0,1] neg_hi:[0,0,1]
	v_cvt_pk_f16_f32 v10, v10, v11
	v_cvt_pk_f16_f32 v11, v12, v13
	v_cvt_pk_f16_f32 v12, v4, v5
	v_cvt_pk_f16_f32 v13, v2, v3
	v_mov_b32_e32 v2, s45
	ds_write_b128 v16, v[10:13] offset:20480
	s_waitcnt lgkmcnt(0)
	s_barrier
	ds_read_b64 v[10:11], v2
	ds_read_b128 v[26:29], v24 offset:29696
	v_add_u32_e32 v38, s48, v17
	ds_read_b128 v[2:5], v25 offset:29696
	v_ashrrev_i32_e32 v39, 31, v38
	s_waitcnt lgkmcnt(2)
	v_readfirstlane_b32 s26, v10
	v_readfirstlane_b32 s27, v11
	s_add_u32 s26, s26, s28
	s_addc_u32 s27, s27, 0
	s_lshl_b32 s28, s38, 2
	s_add_u32 s26, s26, s28
	s_addc_u32 s27, s27, 0
	global_load_dwordx4 v[10:13], v44, s[26:27] offset:2048
	global_load_dwordx4 v[226:229], v44, s[26:27] offset:2112
	ds_read_b128 v[30:33], v23 offset:20480
	ds_read_b128 v[34:37], v24 offset:29760
	v_lshlrev_b64 v[38:39], 11, v[38:39]
	v_lshl_add_u64 v[38:39], s[18:19], 0, v[38:39]
	v_lshl_add_u64 v[42:43], v[38:39], 0, s[20:21]
	ds_read_b128 v[38:41], v23 offset:20544
	s_waitcnt lgkmcnt(2)
	v_mfma_f32_16x16x32_f16 v[26:29], v[26:29], v[30:33], 0
	v_lshlrev_b32_e32 v8, 1, v6
	v_lshl_add_u64 v[42:43], v[42:43], 0, v[8:9]
	s_lshl_b32 s20, s38, 1
	s_waitcnt lgkmcnt(0)
	v_mfma_f32_16x16x32_f16 v[26:29], v[34:37], v[38:41], v[26:29]
	v_lshl_add_u64 v[42:43], v[42:43], 0, s[20:21]
	s_add_i32 s47, s47, s33
	s_add_i32 s46, s46, s33
	v_mfma_f32_16x16x32_f16 v[2:5], v[2:5], v[30:33], 0
	s_add_i32 s39, s39, s40
	s_cmpk_gt_i32 s47, 0x47f
	s_waitcnt vmcnt(1)
	s_nop 0
	v_mul_f32_e32 v8, v28, v12
	v_mul_f32_e32 v11, v27, v11
	v_fma_mixlo_f16 v26, v26, v10, 0
	v_pk_mov_b32 v[10:11], v[10:11], v[8:9] op_sel:[1,0]
	v_fma_mixlo_f16 v12, v29, v13, 0
	v_cvt_pk_f16_f32 v8, v10, v11
	v_pack_b32_f16 v10, v26, v8
	v_alignbit_b32 v11, v12, v8, 16
	global_store_dwordx2 v[42:43], v[10:11], off
	ds_read_b128 v[26:29], v25 offset:29760
	s_waitcnt lgkmcnt(0)
	v_mfma_f32_16x16x32_f16 v[2:5], v[26:29], v[38:41], v[2:5]
	s_waitcnt vmcnt(1)
	s_nop 6
	v_fma_mixlo_f16 v8, v2, v226, 0
	v_mul_f32_e32 v2, v4, v228
	v_mul_f32_e32 v3, v3, v227
	v_pk_mov_b32 v[2:3], v[2:3], v[2:3] op_sel:[1,0]
	v_fma_mixlo_f16 v4, v5, v229, 0
	v_cvt_pk_f16_f32 v3, v2, v3
	v_pack_b32_f16 v2, v8, v3
	v_alignbit_b32 v3, v4, v3, 16
	global_store_dwordx2 v[42:43], v[2:3], off offset:32
	s_cbranch_scc1 .LBB0_3401

.LBB0_4774:
	s_or_b64 exec, exec, s[22:23]
	v_sub_u32_e32 v8, v26, v8
	v_cvt_f32_i32_e32 v8, v8
	ds_read_b128 v[26:29], v15 offset:2048
	ds_read_b128 v[30:33], v15 offset:2064
	s_lshl_b32 s16, s49, 7
	s_lshl_b32 s24, s49, 8
	v_div_scale_f32 v34, s[22:23], v8, v8, 1.0
	v_rcp_f32_e32 v35, v34
	v_div_scale_f32 v36, vcc, 1.0, v8, 1.0
	v_lshlrev_b32_e32 v44, 2, v6
	v_fma_f32 v37, -v34, v35, 1.0
	v_fmac_f32_e32 v35, v37, v35
	v_mul_f32_e32 v37, v36, v35
	v_fma_f32 v38, -v34, v37, v36
	v_fmac_f32_e32 v37, v38, v35
	v_fma_f32 v34, -v34, v37, v36
	v_div_fmas_f32 v34, v34, v35, v37
	v_div_fixup_f32 v8, v34, v8, 1.0
	s_waitcnt lgkmcnt(1)
	v_pk_fma_f32 v[10:11], v[8:9], v[10:11], v[26:27] op_sel_hi:[0,1,1] neg_lo:[0,0,1] neg_hi:[0,0,1]
	v_pk_fma_f32 v[12:13], v[8:9], v[12:13], v[28:29] op_sel_hi:[0,1,1] neg_lo:[0,0,1] neg_hi:[0,0,1]
	s_waitcnt lgkmcnt(0)
	v_pk_fma_f32 v[4:5], v[8:9], v[4:5], v[30:31] op_sel_hi:[0,1,1] neg_lo:[0,0,1] neg_hi:[0,0,1]
	v_pk_fma_f32 v[2:3], v[8:9], v[2:3], v[32:33] op_sel_hi:[0,1,1] neg_lo:[0,0,1] neg_hi:[0,0,1]
	v_cvt_pk_f16_f32 v10, v10, v11
	v_cvt_pk_f16_f32 v11, v12, v13
	v_cvt_pk_f16_f32 v12, v4, v5
	v_cvt_pk_f16_f32 v13, v2, v3
	v_mov_b32_e32 v2, s45
	ds_write_b128 v16, v[10:13] offset:20480
	s_waitcnt lgkmcnt(0)
	s_barrier
	ds_read_b64 v[10:11], v2
	ds_read_b128 v[26:29], v24 offset:29696
	v_add_u32_e32 v38, s48, v17
	ds_read_b128 v[2:5], v25 offset:29696
	v_ashrrev_i32_e32 v39, 31, v38
	s_waitcnt lgkmcnt(2)
	v_readfirstlane_b32 s22, v10
	v_readfirstlane_b32 s23, v11
	s_add_u32 s22, s22, s24
	s_addc_u32 s23, s23, 0
	s_lshl_b32 s24, s34, 2
	s_add_u32 s22, s22, s24
	s_addc_u32 s23, s23, 0
	global_load_dwordx4 v[10:13], v44, s[22:23] offset:3072
	global_load_dwordx4 v[226:229], v44, s[22:23] offset:3136
	ds_read_b128 v[30:33], v23 offset:20480
	ds_read_b128 v[34:37], v24 offset:29760
	v_lshlrev_b64 v[38:39], 11, v[38:39]
	v_lshl_add_u64 v[38:39], s[14:15], 0, v[38:39]
	v_lshl_add_u64 v[42:43], v[38:39], 0, s[16:17]
	ds_read_b128 v[38:41], v23 offset:20544
	s_waitcnt lgkmcnt(2)
	v_mfma_f32_16x16x32_f16 v[26:29], v[26:29], v[30:33], 0
	v_lshlrev_b32_e32 v8, 1, v6
	v_lshl_add_u64 v[42:43], v[42:43], 0, v[8:9]
	s_lshl_b32 s16, s34, 1
	s_waitcnt lgkmcnt(0)
	v_mfma_f32_16x16x32_f16 v[26:29], v[34:37], v[38:41], v[26:29]
	v_lshl_add_u64 v[42:43], v[42:43], 0, s[16:17]
	s_add_i32 s47, s47, s33
	s_add_i32 s46, s46, s33
	v_mfma_f32_16x16x32_f16 v[2:5], v[2:5], v[30:33], 0
	s_add_i32 s35, s35, s40
	s_cmpk_gt_i32 s47, 0x3ff
	s_waitcnt vmcnt(1)
	s_nop 0
	v_mul_f32_e32 v8, v28, v12
	v_mul_f32_e32 v11, v27, v11
	v_fma_mixlo_f16 v26, v26, v10, 0
	v_pk_mov_b32 v[10:11], v[10:11], v[8:9] op_sel:[1,0]
	v_fma_mixlo_f16 v12, v29, v13, 0
	v_cvt_pk_f16_f32 v8, v10, v11
	v_pack_b32_f16 v10, v26, v8
	v_alignbit_b32 v11, v12, v8, 16
	global_store_dwordx2 v[42:43], v[10:11], off
	ds_read_b128 v[26:29], v25 offset:29760
	s_waitcnt lgkmcnt(0)
	v_mfma_f32_16x16x32_f16 v[2:5], v[26:29], v[38:41], v[2:5]
	s_waitcnt vmcnt(1)
	s_nop 6
	v_fma_mixlo_f16 v8, v2, v226, 0
	v_mul_f32_e32 v2, v4, v228
	v_mul_f32_e32 v3, v3, v227
	v_pk_mov_b32 v[2:3], v[2:3], v[2:3] op_sel:[1,0]
	v_fma_mixlo_f16 v4, v5, v229, 0
	v_cvt_pk_f16_f32 v3, v2, v3
	v_pack_b32_f16 v2, v8, v3
	v_alignbit_b32 v3, v4, v3, 16
	global_store_dwordx2 v[42:43], v[2:3], off offset:32
	s_cbranch_scc1 .LBB0_4803
